# prep phase WcsT fold: workgroup-uniform trig factors gathered once into an LDS strip [m][8] and read with ds_read_b128 at immediate offsets instead of per-lane index math + 8 ds_read_b32 per m (loop b
# speedup vs baseline: 1.0221x; 1.0098x over previous
; __device__ void phase_prep(KParams& p, int bid, int nb, char* smem) {
;     ...
;     for (int i = vb * NTHREADS + tid; i < 4 * 64 * 256; i += nb * NTHREADS) {
;       const int d = i & 255, cg = (i >> 8) & 63, g = i >> 14;
;       float c0_ = 0.f, c1_ = 0.f, c2_ = 0.f, c3_ = 0.f, s0_ = 0.f, s1_ = 0.f, s2_ = 0.f, s3_ = 0.f;
;       const float* wp = p.w_fmix + (size_t)g * 65536 + d;
; #pragma unroll 1
;       for (int mb = 0; mb < 256; mb += 16) {
;         float wv[16];
; #pragma unroll
;         for (int mm = 0; mm < 16; ++mm) wv[mm] = wp[(mb + mm) * 256];
; #pragma unroll
;         for (int mm = 0; mm < 16; ++mm) {
;           const int m = mb + mm;
;           const int p0 = (m * (cg * 4 + 0)) & 255, p1 = (m * (cg * 4 + 1)) & 255, p2 = (m * (cg * 4 + 2)) & 255, p3 = (m * (cg * 4 + 3)) & 255;
;           c0_ += t256[p0] * wv[mm]; s0_ += t256[(p0 - 64) & 255] * wv[mm];
.LBB0_50:
	v_ashrrev_i32_e32 v10, 14, v1
	v_bfe_u32 v2, v1, 8, 6
	v_ashrrev_i32_e32 v11, 31, v10
	v_lshlrev_b32_e32 v31, 6, v2
	v_lshlrev_b64 v[10:11], 18, v[10:11]
	v_or_b32_e32 v33, 16, v31
	v_or_b32_e32 v35, 32, v31
	v_or_b32_e32 v37, 48, v31
	v_mul_u32_u24_e32 v39, 60, v2
	v_mul_u32_u24_e32 v41, 56, v2
	v_mul_u32_u24_e32 v43, 52, v2
	v_mul_u32_u24_e32 v45, 48, v2
	v_mul_u32_u24_e32 v47, 44, v2
	v_mul_u32_u24_e32 v49, 40, v2
	v_mul_u32_u24_e32 v51, 36, v2
	v_lshlrev_b32_e32 v52, 5, v2
	v_mul_u32_u24_e32 v53, 28, v2
	v_mul_u32_u24_e32 v54, 24, v2
	v_mul_u32_u24_e32 v55, 20, v2
	v_lshlrev_b32_e32 v56, 4, v2
	v_mul_u32_u24_e32 v57, 12, v2
	v_lshlrev_b32_e32 v58, 3, v2
	v_lshlrev_b32_e32 v59, 2, v2
	v_lshl_add_u64 v[12:13], v[8:9], 0, v[10:11]
	v_mov_b32_e32 v60, 0
	v_mov_b32_e32 v61, 0
	v_mov_b32_e32 v62, 0
	v_mov_b32_e32 v63, 0
	s_mov_b32 s19, 0
	v_mov_b32_e32 v14, 0
	v_mov_b32_e32 v15, v3
	v_mov_b32_e32 v16, 0
	v_mov_b32_e32 v17, v3
	v_mov_b32_e32 v18, 0
	v_mov_b32_e32 v19, v3
	v_mov_b32_e32 v20, 0
	v_mov_b32_e32 v21, v3
	v_lshlrev_b32_e32 v60, 2, v2
	v_mul_u32_u24_e32 v61, v60, v0
	v_add_u32_e32 v62, v61, v0
	v_add_u32_e32 v63, v62, v0
	v_add_u32_e32 v64, v63, v0
	v_and_b32_e32 v65, 0xff, v61
	v_add_u32_e32 v66, 0xc0, v61
	v_lshlrev_b32_e32 v65, 2, v65
	v_and_b32_e32 v66, 0xff, v66
	v_lshlrev_b32_e32 v66, 2, v66
	v_and_b32_e32 v67, 0xff, v62
	v_add_u32_e32 v68, 0xc0, v62
	v_lshlrev_b32_e32 v67, 2, v67
	v_and_b32_e32 v68, 0xff, v68
	v_lshlrev_b32_e32 v68, 2, v68
	v_and_b32_e32 v69, 0xff, v63
	v_add_u32_e32 v70, 0xc0, v63
	v_lshlrev_b32_e32 v69, 2, v69
	v_and_b32_e32 v70, 0xff, v70
	v_lshlrev_b32_e32 v70, 2, v70
	v_and_b32_e32 v71, 0xff, v64
	v_add_u32_e32 v72, 0xc0, v64
	v_lshlrev_b32_e32 v71, 2, v71
	v_and_b32_e32 v72, 0xff, v72
	v_lshlrev_b32_e32 v72, 2, v72
	ds_read_b32 v74, v65 offset:20480
	ds_read_b32 v75, v67 offset:20480
	ds_read_b32 v76, v66 offset:20480
	ds_read_b32 v77, v68 offset:20480
	ds_read_b32 v78, v69 offset:20480
	ds_read_b32 v79, v71 offset:20480
	ds_read_b32 v80, v70 offset:20480
	ds_read_b32 v81, v72 offset:20480
	v_lshlrev_b32_e32 v60, 5, v0
	s_waitcnt lgkmcnt(0)
	s_barrier
	ds_write_b128 v60, v[74:77] offset:32768
	ds_write_b128 v60, v[78:81] offset:32784
	s_waitcnt lgkmcnt(0)
	s_barrier
	v_mov_b32_e32 v60, 0
.LBB0_51:
	v_add_co_u32_e32 v26, vcc, s15, v12
	global_load_dword v22, v[12:13], off offset:-1024
	global_load_dword v2, v[12:13], off
	v_addc_co_u32_e32 v27, vcc, -1, v13, vcc
	v_add_co_u32_e32 v24, vcc, s16, v12
	s_nop 1
	v_addc_co_u32_e32 v25, vcc, -1, v13, vcc
	v_add_co_u32_e32 v28, vcc, s17, v12
	s_nop 1
	v_addc_co_u32_e32 v29, vcc, -1, v13, vcc
	global_load_dword v50, v[26:27], off offset:-3072
	global_load_dword v48, v[26:27], off offset:-2048
	global_load_dword v44, v[26:27], off offset:-1024
	global_load_dword v34, v[28:29], off offset:-3072
	global_load_dword v32, v[28:29], off offset:-2048
	s_nop 0
	global_load_dword v28, v[28:29], off offset:-1024
	s_nop 0
	global_load_dword v46, v[24:25], off offset:-4096
	global_load_dword v42, v[24:25], off offset:-3072
	global_load_dword v40, v[24:25], off offset:-2048
	global_load_dword v38, v[24:25], off offset:-1024
	global_load_dword v36, v[24:25], off
	global_load_dword v30, v[12:13], off offset:-4096
	global_load_dword v26, v[12:13], off offset:-3072
	s_nop 0
	global_load_dword v24, v[12:13], off offset:-2048
	ds_read_b128 v[64:67], v60 offset:32768
	ds_read_b128 v[68:71], v60 offset:32784
	ds_read_b128 v[72:75], v60 offset:32800
	ds_read_b128 v[76:79], v60 offset:32816
	ds_read_b128 v[80:83], v60 offset:32832
	ds_read_b128 v[84:87], v60 offset:32848
	ds_read_b128 v[88:91], v60 offset:32864
	ds_read_b128 v[92:95], v60 offset:32880
	ds_read_b128 v[96:99], v60 offset:32896
	ds_read_b128 v[100:103], v60 offset:32912
	ds_read_b128 v[104:107], v60 offset:32928
	ds_read_b128 v[108:111], v60 offset:32944
	ds_read_b128 v[112:115], v60 offset:32960
	ds_read_b128 v[116:119], v60 offset:32976
	ds_read_b128 v[120:123], v60 offset:32992
	ds_read_b128 v[124:127], v60 offset:33008
	ds_read_b128 v[128:131], v60 offset:33024
	ds_read_b128 v[132:135], v60 offset:33040
	ds_read_b128 v[136:139], v60 offset:33056
	ds_read_b128 v[140:143], v60 offset:33072
	ds_read_b128 v[144:147], v60 offset:33088
	ds_read_b128 v[148:151], v60 offset:33104
	ds_read_b128 v[152:155], v60 offset:33120
	ds_read_b128 v[156:159], v60 offset:33136
	ds_read_b128 v[160:163], v60 offset:33152
	ds_read_b128 v[164:167], v60 offset:33168
	ds_read_b128 v[168:171], v60 offset:33184
	ds_read_b128 v[172:175], v60 offset:33200
	ds_read_b128 v[196:199], v60 offset:33216
	ds_read_b128 v[200:203], v60 offset:33232
	ds_read_b128 v[204:207], v60 offset:33248
	ds_read_b128 v[208:211], v60 offset:33264
	s_add_i32 s20, s19, 16
	v_lshl_add_u64 v[12:13], v[12:13], 0, s[10:11]
	s_waitcnt vmcnt(0) lgkmcnt(0)
; __device__ void phase_prep(KParams& p, int bid, int nb, char* smem) {
;     ...
;         for (int mm = 0; mm < 16; ++mm) wv[mm] = wp[(mb + mm) * 256];
; #pragma unroll
;         for (int mm = 0; mm < 16; ++mm) {
;           const int m = mb + mm;
;           const int p0 = (m * (cg * 4 + 0)) & 255, p1 = (m * (cg * 4 + 1)) & 255, p2 = (m * (cg * 4 + 2)) & 255, p3 = (m * (cg * 4 + 3)) & 255;
;           c0_ += t256[p0] * wv[mm]; s0_ += t256[(p0 - 64) & 255] * wv[mm];
;           c1_ += t256[p1] * wv[mm]; s1_ += t256[(p1 - 64) & 255] * wv[mm];
;           c2_ += t256[p2] * wv[mm]; s2_ += t256[(p2 - 64) & 255] * wv[mm];
;           c3_ += t256[p3] * wv[mm]; s3_ += t256[(p3 - 64) & 255] * wv[mm];
;         }
;       }
;       {
;         bf16_t* wc = p.WcsT + ((size_t)g * 512 + d) * 256 + cg * 4;
;         bf16_t* ws_ = p.WcsT + ((size_t)g * 512 + 256 + d) * 256 + cg * 4;
;         uint2 oc, os;
;         oc.x = pack2(c0_ * scale, c1_ * scale); oc.y = pack2(c2_ * scale, c3_ * scale);
;         os.x = pack2(s0_ * scale, s1_ * scale); os.y = pack2(s2_ * scale, s3_ * scale);
;         *reinterpret_cast<uint2*>(wc) = oc;
;         *reinterpret_cast<uint2*>(ws_) = os;
;       }
	v_add_u32_e32 v60, 0x200, v60
	v_pk_fma_f32 v[20:21], v[50:51], v[64:65], v[20:21] op_sel_hi:[0,1,1]
	v_pk_fma_f32 v[18:19], v[50:51], v[66:67], v[18:19] op_sel_hi:[0,1,1]
	v_pk_fma_f32 v[16:17], v[50:51], v[68:69], v[16:17] op_sel_hi:[0,1,1]
	v_pk_fma_f32 v[14:15], v[50:51], v[70:71], v[14:15] op_sel_hi:[0,1,1]
	v_pk_fma_f32 v[20:21], v[48:49], v[72:73], v[20:21] op_sel_hi:[0,1,1]
	v_pk_fma_f32 v[18:19], v[48:49], v[74:75], v[18:19] op_sel_hi:[0,1,1]
	v_pk_fma_f32 v[16:17], v[48:49], v[76:77], v[16:17] op_sel_hi:[0,1,1]
	v_pk_fma_f32 v[14:15], v[48:49], v[78:79], v[14:15] op_sel_hi:[0,1,1]
	v_pk_fma_f32 v[20:21], v[44:45], v[80:81], v[20:21] op_sel_hi:[0,1,1]
	v_pk_fma_f32 v[18:19], v[44:45], v[82:83], v[18:19] op_sel_hi:[0,1,1]
	v_pk_fma_f32 v[16:17], v[44:45], v[84:85], v[16:17] op_sel_hi:[0,1,1]
	v_pk_fma_f32 v[14:15], v[44:45], v[86:87], v[14:15] op_sel_hi:[0,1,1]
	v_pk_fma_f32 v[20:21], v[46:47], v[88:89], v[20:21] op_sel_hi:[0,1,1]
	v_pk_fma_f32 v[18:19], v[46:47], v[90:91], v[18:19] op_sel_hi:[0,1,1]
	v_pk_fma_f32 v[16:17], v[46:47], v[92:93], v[16:17] op_sel_hi:[0,1,1]
	v_pk_fma_f32 v[14:15], v[46:47], v[94:95], v[14:15] op_sel_hi:[0,1,1]
	v_pk_fma_f32 v[20:21], v[42:43], v[96:97], v[20:21] op_sel_hi:[0,1,1]
	v_pk_fma_f32 v[18:19], v[42:43], v[98:99], v[18:19] op_sel_hi:[0,1,1]
	v_pk_fma_f32 v[16:17], v[42:43], v[100:101], v[16:17] op_sel_hi:[0,1,1]
	v_pk_fma_f32 v[14:15], v[42:43], v[102:103], v[14:15] op_sel_hi:[0,1,1]
	v_pk_fma_f32 v[20:21], v[40:41], v[104:105], v[20:21] op_sel_hi:[0,1,1]
	v_pk_fma_f32 v[18:19], v[40:41], v[106:107], v[18:19] op_sel_hi:[0,1,1]
	v_pk_fma_f32 v[16:17], v[40:41], v[108:109], v[16:17] op_sel_hi:[0,1,1]
	v_pk_fma_f32 v[14:15], v[40:41], v[110:111], v[14:15] op_sel_hi:[0,1,1]
	v_pk_fma_f32 v[20:21], v[38:39], v[112:113], v[20:21] op_sel_hi:[0,1,1]
	v_pk_fma_f32 v[18:19], v[38:39], v[114:115], v[18:19] op_sel_hi:[0,1,1]
	v_pk_fma_f32 v[16:17], v[38:39], v[116:117], v[16:17] op_sel_hi:[0,1,1]
	v_pk_fma_f32 v[14:15], v[38:39], v[118:119], v[14:15] op_sel_hi:[0,1,1]
	v_pk_fma_f32 v[20:21], v[36:37], v[120:121], v[20:21] op_sel_hi:[0,1,1]
	v_pk_fma_f32 v[18:19], v[36:37], v[122:123], v[18:19] op_sel_hi:[0,1,1]
	v_pk_fma_f32 v[16:17], v[36:37], v[124:125], v[16:17] op_sel_hi:[0,1,1]
	v_pk_fma_f32 v[14:15], v[36:37], v[126:127], v[14:15] op_sel_hi:[0,1,1]
	v_pk_fma_f32 v[20:21], v[34:35], v[128:129], v[20:21] op_sel_hi:[0,1,1]
	v_pk_fma_f32 v[18:19], v[34:35], v[130:131], v[18:19] op_sel_hi:[0,1,1]
	v_pk_fma_f32 v[16:17], v[34:35], v[132:133], v[16:17] op_sel_hi:[0,1,1]
	v_pk_fma_f32 v[14:15], v[34:35], v[134:135], v[14:15] op_sel_hi:[0,1,1]
	v_pk_fma_f32 v[20:21], v[32:33], v[136:137], v[20:21] op_sel_hi:[0,1,1]
	v_pk_fma_f32 v[18:19], v[32:33], v[138:139], v[18:19] op_sel_hi:[0,1,1]
	v_pk_fma_f32 v[16:17], v[32:33], v[140:141], v[16:17] op_sel_hi:[0,1,1]
	v_pk_fma_f32 v[14:15], v[32:33], v[142:143], v[14:15] op_sel_hi:[0,1,1]
	v_pk_fma_f32 v[20:21], v[28:29], v[144:145], v[20:21] op_sel_hi:[0,1,1]
	v_pk_fma_f32 v[18:19], v[28:29], v[146:147], v[18:19] op_sel_hi:[0,1,1]
	v_pk_fma_f32 v[16:17], v[28:29], v[148:149], v[16:17] op_sel_hi:[0,1,1]
	v_pk_fma_f32 v[14:15], v[28:29], v[150:151], v[14:15] op_sel_hi:[0,1,1]
	v_pk_fma_f32 v[20:21], v[30:31], v[152:153], v[20:21] op_sel_hi:[0,1,1]
	v_pk_fma_f32 v[18:19], v[30:31], v[154:155], v[18:19] op_sel_hi:[0,1,1]
	v_pk_fma_f32 v[16:17], v[30:31], v[156:157], v[16:17] op_sel_hi:[0,1,1]
	v_pk_fma_f32 v[14:15], v[30:31], v[158:159], v[14:15] op_sel_hi:[0,1,1]
	v_pk_fma_f32 v[20:21], v[26:27], v[160:161], v[20:21] op_sel_hi:[0,1,1]
	v_pk_fma_f32 v[18:19], v[26:27], v[162:163], v[18:19] op_sel_hi:[0,1,1]
	v_pk_fma_f32 v[16:17], v[26:27], v[164:165], v[16:17] op_sel_hi:[0,1,1]
	v_pk_fma_f32 v[14:15], v[26:27], v[166:167], v[14:15] op_sel_hi:[0,1,1]
	v_pk_fma_f32 v[20:21], v[24:25], v[168:169], v[20:21] op_sel_hi:[0,1,1]
	v_pk_fma_f32 v[18:19], v[24:25], v[170:171], v[18:19] op_sel_hi:[0,1,1]
	v_pk_fma_f32 v[16:17], v[24:25], v[172:173], v[16:17] op_sel_hi:[0,1,1]
	v_pk_fma_f32 v[14:15], v[24:25], v[174:175], v[14:15] op_sel_hi:[0,1,1]
	v_pk_fma_f32 v[20:21], v[22:23], v[196:197], v[20:21] op_sel_hi:[0,1,1]
	v_pk_fma_f32 v[18:19], v[22:23], v[198:199], v[18:19] op_sel_hi:[0,1,1]
	v_pk_fma_f32 v[16:17], v[22:23], v[200:201], v[16:17] op_sel_hi:[0,1,1]
	v_pk_fma_f32 v[14:15], v[22:23], v[202:203], v[14:15] op_sel_hi:[0,1,1]
	v_pk_fma_f32 v[20:21], v[2:3], v[204:205], v[20:21] op_sel_hi:[0,1,1]
	v_pk_fma_f32 v[18:19], v[2:3], v[206:207], v[18:19] op_sel_hi:[0,1,1]
	v_pk_fma_f32 v[16:17], v[2:3], v[208:209], v[16:17] op_sel_hi:[0,1,1]
	v_pk_fma_f32 v[14:15], v[2:3], v[210:211], v[14:15] op_sel_hi:[0,1,1]
	s_cmpk_gt_u32 s19, 0xef
	s_mov_b32 s19, s20
	s_cbranch_scc0 .LBB0_51
	v_lshrrev_b32_e32 v2, 5, v1
	v_lshl_add_u64 v[10:11], v[4:5], 0, v[10:11]
	v_and_b32_e32 v2, 0x1f8, v2
	v_pk_mul_f32 v[12:13], v[20:21], s[14:15] op_sel_hi:[1,0]
	v_pk_mul_f32 v[16:17], v[16:17], s[14:15] op_sel_hi:[1,0]
	v_lshl_add_u64 v[10:11], v[10:11], 0, v[2:3]
	v_cvt_pk_bf16_f32 v12, v12, v13
	v_cvt_pk_bf16_f32 v13, v16, v17
	global_store_dwordx2 v[10:11], v[12:13], off
	v_add_co_u32_e32 v10, vcc, 0x20000, v10
	v_add_u32_e32 v1, s3, v1
	s_nop 0
	v_addc_co_u32_e32 v11, vcc, 0, v11, vcc
	v_pk_mul_f32 v[16:17], v[18:19], s[14:15] op_sel_hi:[1,0]
	v_pk_mul_f32 v[14:15], v[14:15], s[14:15] op_sel_hi:[1,0]
	v_cmp_lt_i32_e32 vcc, s18, v1
	v_cvt_pk_bf16_f32 v16, v16, v17
	v_cvt_pk_bf16_f32 v17, v14, v15
	s_or_b64 s[8:9], vcc, s[8:9]
	global_store_dwordx2 v[10:11], v[16:17], off
	s_andn2_b64 exec, exec, s[8:9]
	s_cbranch_execnz .LBB0_50
